# c7
# speedup vs baseline: 1.0110x; 1.0017x over previous
.LBB2_88:
	s_or_b64 exec, exec, s[10:11]
	v_mov_b32_e32 v33, v24
	v_mov_b32_e32 v24, v25
	v_mov_b32_e32 v25, v26
	v_pk_add_f32 v[184:185], v[68:69], v[24:25]
	v_mov_b32_e32 v24, v82
	v_mov_b32_e32 v25, v70
	v_mov_b32_e32 v26, v55
	v_pk_add_f32 v[180:181], v[24:25], v[26:27]
	v_mov_b32_e32 v24, v83
	v_mov_b32_e32 v25, v84
	v_mov_b32_e32 v32, v23
	v_pk_add_f32 v[186:187], v[24:25], v[56:57]
	v_mov_b32_e32 v24, v85
	v_mov_b32_e32 v25, v86
	v_pk_add_f32 v[182:183], v[66:67], v[32:33]
	v_pk_add_f32 v[188:189], v[24:25], v[58:59]
	s_waitcnt lgkmcnt(1)
	v_mfma_f32_32x32x16_f16 v[2:17], v[116:119], v[60:63], v[2:17]
	s_waitcnt lgkmcnt(0)
	v_mfma_f32_32x32x16_f16 v[2:17], v[112:115], v[28:31], v[2:17]
	s_mul_i32 s2, s2, s40
	s_bfe_u32 s28, s42, 0x30003
	s_add_i32 s2, s2, s41
	s_lshl_b32 s10, s28, 17
	s_and_b32 s2, s2, 7
	s_add_i32 s10, s33, s10
	s_nop 5
	v_mov_b32_e32 v17, 15
	s_lshl_b32 s2, s2, 12
	v_lshlrev_b32_sdwa v17, v17, v193 dst_sel:DWORD dst_unused:UNUSED_PAD src0_sel:DWORD src1_sel:BYTE_1
	v_add_lshl_u32 v23, v192, v191, 10
	s_add_i32 s2, s2, s10
	v_add3_u32 v17, s2, v17, v23
	s_movk_i32 s10, 0xfc00
	v_add3_u32 v24, v17, v1, s10
	v_ashrrev_i32_e32 v25, 31, v24
	v_lshl_add_u64 v[26:27], v[24:25], 2, s[14:15]
	v_lshlrev_b64 v[192:193], 4, v[24:25]
	v_lshlrev_b32_e32 v23, 15, v195
	v_add_lshl_u32 v24, v196, v194, 10
	v_add3_u32 v23, s2, v23, v24
	s_mov_b32 s29, 0xffff7c00
	v_add3_u32 v24, v23, v1, s29
	s_mov_b64 s[10:11], 0x280
	v_ashrrev_i32_e32 v25, 31, v24
	v_lshl_add_u64 v[32:33], v[26:27], 0, s[10:11]
	v_lshl_add_u64 v[26:27], v[24:25], 2, s[14:15]
	v_lshlrev_b64 v[196:197], 4, v[24:25]
	v_lshlrev_b32_e32 v24, 15, v198
	v_add_lshl_u32 v25, v64, v191, 10
	v_add3_u32 v28, s2, v24, v25
	v_add3_u32 v24, v28, v1, s29
	v_add_u32_e32 v217, 0xfffffc80, v17
	s_lshl_b32 s2, s28, 7
	v_lshlrev_b32_e32 v17, 5, v214
	v_ashrrev_i32_e32 v25, 31, v24
	v_or3_b32 v17, v190, s2, v17
	v_lshl_add_u64 v[194:195], v[26:27], 0, s[10:11]
	v_lshl_add_u64 v[26:27], v[24:25], 2, s[14:15]
	v_add3_u32 v17, v17, s3, v213
	s_mov_b32 s40, 2
	v_lshl_add_u64 v[198:199], v[26:27], 0, s[10:11]
	v_lshlrev_b64 v[200:201], 4, v[24:25]
	v_add_u32_e32 v215, 0xffff7c80, v28
	v_add_u32_e32 v216, 0xffff7c80, v23
	v_lshl_add_u32 v213, v17, 10, s33
	s_mov_b64 s[10:11], 0x100
	v_mbcnt_lo_u32_b32 v24, -1, 0
	v_mbcnt_hi_u32_b32 v24, -1, v24
	v_and_b32_e32 v24, 31, v24
	v_cmp_eq_u32_e64 s[46:47], 0, v24
	v_cmp_eq_u32_e64 s[48:49], 31, v24
	v_mul_u32_u24_e32 v25, 11, v24
	v_lshrrev_b32_e32 v25, 5, v25
	v_mul_u32_u24_e32 v25, 3, v25
	v_sub_u32_e32 v24, v24, v25
	v_mul_u32_u24_e32 v26, 12, v24
	v_cndmask_b32_e64 v26, v26, 12, s[46:47]
	v_add_u32_e32 v25, 2, v24
	v_mul_u32_u24_e32 v27, 11, v25
	v_lshrrev_b32_e32 v27, 5, v27
	v_mul_u32_u24_e32 v27, 3, v27
	v_sub_u32_e32 v25, v25, v27
	v_mul_u32_u24_e32 v25, 12, v25
	v_add_u32_e32 v25, -12, v25
	v_add_u32_e32 v24, 1, v24
	v_mul_u32_u24_e32 v27, 11, v24
	v_lshrrev_b32_e32 v27, 5, v27
	v_mul_u32_u24_e32 v27, 3, v27
	v_sub_u32_e32 v24, v24, v27
	v_mul_u32_u24_e32 v24, 12, v24
	v_add_u32_e32 v24, 0xffffffe8, v24
	v_cndmask_b32_e64 v24, v24, -12, s[48:49]
	v_add_u32_e32 v230, v208, v25
	v_add_u32_e32 v231, v208, v26
	v_add_u32_e32 v232, v208, v24
	v_add_u32_e32 v233, v210, v25
	v_add_u32_e32 v234, v210, v26
	v_add_u32_e32 v235, v210, v24
	v_add_u32_e32 v236, v211, v25
	v_add_u32_e32 v237, v211, v26
	v_add_u32_e32 v238, v211, v24
	s_barrier

.LBB2_95:
	s_or_b64 exec, exec, s[34:35]
	v_mfma_f32_32x32x16_f16 v[56:71], v[168:171], v[72:75], v[56:71]
	ds_read_b128 v[218:221], v205 offset:3168
	ds_read_b128 v[222:225], v207 offset:3168
	v_mfma_f32_32x32x16_f16 v[72:87], v[176:179], v[72:75], 0
	s_waitcnt lgkmcnt(3)
	v_mfma_f32_32x32x16_f16 v[56:71], v[160:163], v[100:103], v[56:71]
	v_mfma_f32_32x32x16_f16 v[72:87], v[172:175], v[100:103], v[72:87]
	v_mfma_f32_32x32x16_f16 v[56:71], v[164:167], v[96:99], v[56:71]
	v_mfma_f32_32x32x16_f16 v[72:87], v[168:171], v[96:99], v[72:87]
	ds_read_b128 v[96:99], v205 offset:6336
	ds_read_b128 v[100:103], v207 offset:6336
	s_waitcnt lgkmcnt(4)
	v_mfma_f32_32x32x16_f16 v[56:71], v[156:159], v[92:95], v[56:71]
	v_mfma_f32_32x32x16_f16 v[72:87], v[160:163], v[92:95], v[72:87]
	v_add_f32_e32 v14, v187, v14
	v_add_f32_e32 v15, v188, v15
	v_add_f32_e32 v12, v180, v12
	v_add_f32_e32 v13, v186, v13
	s_waitcnt lgkmcnt(3)
	v_mfma_f32_32x32x16_f16 v[72:87], v[164:167], v[218:221], v[72:87]
	v_max_f32_e32 v14, 0, v14
	v_max_f32_e32 v15, 0, v15
	v_max_f32_e32 v12, 0, v12
	v_max_f32_e32 v13, 0, v13
	v_cvt_pk_f16_f32 v15, v14, v15
	v_cvt_pk_f16_f32 v14, v12, v13
	v_add_f32_e32 v12, v189, v16
	v_max_f32_e32 v16, 0, v12
	v_add_f32_e32 v12, v184, v46
	v_add_f32_e32 v13, v185, v47
	v_max_f32_e32 v12, 0, v12
	v_max_f32_e32 v13, 0, v13
	v_cvt_pk_f16_f32 v13, v12, v13
	v_add_f32_e32 v12, v182, v44
	v_add_f32_e32 v44, v183, v45
	s_waitcnt lgkmcnt(2)
	v_mfma_f32_32x32x16_f16 v[72:87], v[156:159], v[222:225], v[72:87]
	v_max_f32_e32 v12, 0, v12
	v_max_f32_e32 v44, 0, v44
	v_cvt_pk_f16_f32 v12, v12, v44
	v_add_f32_e32 v44, v181, v48
	ds_read_b128 v[92:95], v205 offset:7392
	ds_read_b128 v[226:229], v207 offset:7392
	v_add_u32_e32 v48, v1, v213
	v_max_f32_e32 v55, 0, v44
	v_add_u32_e32 v44, 32, v48
	v_ashrrev_i32_e32 v45, 31, v44
	v_permlane32_swap_b32_e32 v12, v14
	v_permlane32_swap_b32_e32 v13, v15
	v_permlane32_swap_b32_e32 v55, v16
	v_lshl_add_u64 v[46:47], v[44:45], 4, s[16:17]
	global_store_dwordx4 v[46:47], v[12:15], off sc1
	s_nop 1
	v_cvt_pk_f16_f32 v14, v55, v16
	v_lshl_add_u64 v[12:13], v[44:45], 2, s[18:19]
	global_store_dword v[12:13], v14, off sc1
	s_waitcnt lgkmcnt(3)
	v_mfma_f32_32x32x16_f16 v[56:71], v[136:139], v[96:99], v[56:71]
	ds_read_b128 v[96:99], v205 offset:8448
	ds_read_b128 v[180:183], v207 offset:8448
	s_waitcnt lgkmcnt(4)
	v_mfma_f32_32x32x16_f16 v[56:71], v[140:143], v[100:103], v[56:71]
	s_waitcnt lgkmcnt(3)
	v_mfma_f32_32x32x16_f16 v[56:71], v[120:123], v[92:95], v[56:71]
	ds_read_b128 v[12:15], v205 offset:9504
	ds_read_b128 v[44:47], v207 offset:9504
	v_mfma_f32_32x32x16_f16 v[72:87], v[136:139], v[92:95], v[72:87]
	s_waitcnt lgkmcnt(4)
	v_mfma_f32_32x32x16_f16 v[56:71], v[152:155], v[226:229], v[56:71]
	v_mfma_f32_32x32x16_f16 v[72:87], v[140:143], v[226:229], v[72:87]
	s_waitcnt lgkmcnt(3)
	v_mfma_f32_32x32x16_f16 v[56:71], v[148:151], v[96:99], v[56:71]
	v_mfma_f32_32x32x16_f16 v[72:87], v[120:123], v[96:99], v[72:87]
	ds_read_b128 v[100:103], v205 offset:12672
	ds_read_b128 v[96:99], v207 offset:12672
	s_waitcnt vmcnt(3)
	ds_write_b128 v208, v[88:91] offset:38032
	s_waitcnt vmcnt(2)
	ds_write_b32 v230, v49 offset:38564
	s_waitcnt lgkmcnt(6)
	v_mfma_f32_32x32x16_f16 v[56:71], v[144:147], v[180:183], v[56:71]
	v_mfma_f32_32x32x16_f16 v[72:87], v[152:155], v[180:183], v[72:87]
	ds_write_b32 v231, v49 offset:38552
	ds_write_b32 v232, v49 offset:38576
	s_waitcnt lgkmcnt(5)
	v_mfma_f32_32x32x16_f16 v[72:87], v[148:151], v[12:15], v[72:87]
	ds_read_b128 v[92:95], v205 offset:13728
	ds_read_b128 v[12:15], v207 offset:13728
	s_waitcnt lgkmcnt(6)
	v_mfma_f32_32x32x16_f16 v[72:87], v[144:147], v[44:47], v[72:87]
	s_waitcnt lgkmcnt(5)
	v_mfma_f32_32x32x16_f16 v[56:71], v[132:135], v[100:103], v[56:71]
	ds_read_b128 v[88:91], v205 offset:14784
	ds_read_b128 v[44:47], v207 offset:14784
	s_waitcnt lgkmcnt(6)
	v_mfma_f32_32x32x16_f16 v[56:71], v[108:111], v[96:99], v[56:71]
	s_and_saveexec_b64 s[34:35], s[0:1]
	s_cbranch_execz .LBB2_104
	ds_write_b128 v210, v[28:31] offset:38032
	ds_write_b32 v233, v23 offset:38564
	ds_write_b32 v234, v23 offset:38552
	ds_write_b32 v235, v23 offset:38576
.LBB2_104:
	s_or_b64 exec, exec, s[34:35]
	s_waitcnt lgkmcnt(3)
	v_mfma_f32_32x32x16_f16 v[56:71], v[128:131], v[92:95], v[56:71]
	v_mfma_f32_32x32x16_f16 v[72:87], v[132:135], v[92:95], v[72:87]
	ds_read_b128 v[92:95], v205 offset:15840
	ds_read_b128 v[28:31], v207 offset:15840
	s_waitcnt lgkmcnt(4)
	v_mfma_f32_32x32x16_f16 v[56:71], v[124:127], v[12:15], v[56:71]
	v_mfma_f32_32x32x16_f16 v[72:87], v[108:111], v[12:15], v[72:87]
	s_waitcnt lgkmcnt(3)
	s_and_saveexec_b64 s[34:35], s[8:9]
	s_cbranch_execz .LBB2_109
	ds_write_b128 v211, v[24:27] offset:38032
	ds_write_b32 v236, v17 offset:38564
	ds_write_b32 v237, v17 offset:38552
	ds_write_b32 v238, v17 offset:38576
.LBB2_109:
	s_or_b64 exec, exec, s[34:35]
	s_waitcnt lgkmcnt(0)
	s_barrier
	ds_read_b128 v[24:27], v205 offset:38016
	ds_read_b128 v[12:15], v205 offset:39072
	v_mfma_f32_32x32x16_f16 v[56:71], v[116:119], v[88:91], v[56:71]
	v_mfma_f32_32x32x16_f16 v[72:87], v[128:131], v[88:91], v[72:87]
	v_mfma_f32_32x32x16_f16 v[56:71], v[112:115], v[44:47], v[56:71]
	v_mfma_f32_32x32x16_f16 v[72:87], v[124:127], v[44:47], v[72:87]
	v_mfma_f32_32x32x16_f16 v[72:87], v[116:119], v[92:95], v[72:87]
	v_mfma_f32_32x32x16_f16 v[72:87], v[112:115], v[28:31], v[72:87]
	s_waitcnt lgkmcnt(1)
	v_mfma_f32_32x32x16_f16 v[88:103], v[176:179], v[24:27], 0
	ds_read_b128 v[24:27], v207 offset:38016
	ds_read_b128 v[184:187], v205 offset:40128
	ds_read_b128 v[188:191], v207 offset:39072
	ds_read_b128 v[180:183], v207 offset:40128
	v_mov_b32_e32 v214, 0
	v_mov_b32_e32 v44, 0
	v_mov_b32_e32 v45, 0
	v_mov_b32_e32 v46, 0
	v_mov_b32_e32 v47, 0
	v_mov_b32_e32 v71, 0
	s_waitcnt lgkmcnt(3)
	v_mfma_f32_32x32x16_f16 v[88:103], v[172:175], v[24:27], v[88:103]
	s_and_saveexec_b64 s[34:35], s[28:29]
	s_cbranch_execz .LBB2_111
	v_lshl_add_u64 v[16:17], s[20:21], 0, v[200:201]
	global_load_dwordx4 v[44:47], v[16:17], off offset:2560
	global_load_dword v214, v[198:199], off

.LBB2_115:
	s_or_b64 exec, exec, s[28:29]
	v_add_f32_e32 v49, v19, v40
	v_add_f32_e32 v55, v20, v41
	v_add_f32_e32 v54, v54, v11
	v_add_f32_e32 v39, v18, v39
	v_add_f32_e32 v222, v21, v42
	v_add_f32_e32 v223, v22, v43
	v_add_f32_e32 v7, v50, v7
	v_add_f32_e32 v224, v51, v8
	v_add_f32_e32 v225, v52, v9
	v_add_f32_e32 v226, v53, v10
	v_mfma_f32_32x32x16_f16 v[88:103], v[168:171], v[12:15], v[88:103]
	ds_read_b128 v[40:43], v205 offset:41184
	ds_read_b128 v[50:53], v207 offset:41184
	v_mfma_f32_32x32x16_f16 v[240:255], v[176:179], v[12:15], 0
	s_waitcnt lgkmcnt(3)
	v_mfma_f32_32x32x16_f16 v[88:103], v[160:163], v[188:191], v[88:103]
	v_mfma_f32_32x32x16_f16 v[240:255], v[172:175], v[188:191], v[240:255]
	v_mfma_f32_32x32x16_f16 v[88:103], v[164:167], v[184:187], v[88:103]
	v_mfma_f32_32x32x16_f16 v[240:255], v[168:171], v[184:187], v[240:255]
	ds_read_b128 v[184:187], v205 offset:44352
	ds_read_b128 v[188:191], v207 offset:44352
	s_waitcnt lgkmcnt(4)
	v_mfma_f32_32x32x16_f16 v[88:103], v[156:159], v[180:183], v[88:103]
	v_mfma_f32_32x32x16_f16 v[240:255], v[160:163], v[180:183], v[240:255]
	v_add_f32_e32 v84, v225, v84
	v_add_f32_e32 v85, v226, v85
	s_waitcnt lgkmcnt(3)
	v_mfma_f32_32x32x16_f16 v[240:255], v[164:167], v[40:43], v[240:255]
	v_add_f32_e32 v40, 0, v85
	v_max_f32_e32 v84, 0, v84
	v_max_f32_e32 v40, 0, v40
	v_cvt_pk_f16_f32 v43, v84, v40
	v_add_f32_e32 v7, v7, v82
	v_add_f32_e32 v40, v224, v83
	v_max_f32_e32 v7, 0, v7
	v_max_f32_e32 v40, 0, v40
	v_cvt_pk_f16_f32 v42, v7, v40
	v_add_f32_e32 v40, v55, v68
	v_add_f32_e32 v41, v222, v69
	v_max_f32_e32 v40, 0, v40
	v_max_f32_e32 v41, 0, v41
	s_waitcnt lgkmcnt(2)
	v_mfma_f32_32x32x16_f16 v[240:255], v[156:159], v[50:53], v[240:255]
	v_cvt_pk_f16_f32 v41, v40, v41
	v_add_f32_e32 v39, v39, v66
	v_add_f32_e32 v40, v49, v67
	v_max_f32_e32 v39, 0, v39
	v_max_f32_e32 v40, 0, v40
	ds_read_b128 v[180:183], v205 offset:45408
	ds_read_b128 v[218:221], v207 offset:45408
	v_add_f32_e32 v7, v54, v86
	v_cvt_pk_f16_f32 v40, v39, v40
	v_add_f32_e32 v39, v223, v70
	v_add_u32_e32 v48, 64, v48
	v_max_f32_e32 v7, 0, v7
	v_max_f32_e32 v39, 0, v39
	v_ashrrev_i32_e32 v49, 31, v48
	v_permlane32_swap_b32_e32 v40, v42
	v_permlane32_swap_b32_e32 v41, v43
	v_permlane32_swap_b32_e32 v39, v7
	v_lshl_add_u64 v[50:51], v[48:49], 4, s[16:17]
	global_store_dwordx4 v[50:51], v[40:43], off sc1
	v_cvt_pk_f16_f32 v7, v39, v7
	s_nop 0
	v_lshl_add_u64 v[40:41], v[48:49], 2, s[18:19]
	global_store_dword v[40:41], v7, off sc1
	s_waitcnt lgkmcnt(3)
	v_mfma_f32_32x32x16_f16 v[88:103], v[136:139], v[184:187], v[88:103]
	ds_read_b128 v[52:55], v205 offset:46464
	ds_read_b128 v[66:69], v207 offset:46464
	s_waitcnt lgkmcnt(4)
	v_mfma_f32_32x32x16_f16 v[88:103], v[140:143], v[188:191], v[88:103]
	s_waitcnt lgkmcnt(3)
	v_mfma_f32_32x32x16_f16 v[88:103], v[120:123], v[180:183], v[88:103]
	ds_read_b128 v[48:51], v205 offset:47520
	ds_read_b128 v[40:43], v207 offset:47520
	v_mfma_f32_32x32x16_f16 v[240:255], v[136:139], v[180:183], v[240:255]
	s_waitcnt lgkmcnt(4)
	v_mfma_f32_32x32x16_f16 v[88:103], v[152:155], v[218:221], v[88:103]
	v_mfma_f32_32x32x16_f16 v[240:255], v[140:143], v[218:221], v[240:255]
	s_waitcnt lgkmcnt(3)
	v_mfma_f32_32x32x16_f16 v[88:103], v[148:151], v[52:55], v[88:103]
	v_mfma_f32_32x32x16_f16 v[240:255], v[120:123], v[52:55], v[240:255]
	ds_read_b128 v[52:55], v205 offset:50688
	ds_read_b128 v[82:85], v207 offset:50688
	s_waitcnt vmcnt(3)
	ds_write_b128 v208, v[44:47] offset:16
	s_waitcnt vmcnt(2)
	ds_write_b32 v230, v214 offset:548
	s_waitcnt lgkmcnt(6)
	v_mfma_f32_32x32x16_f16 v[88:103], v[144:147], v[66:69], v[88:103]
	v_mfma_f32_32x32x16_f16 v[240:255], v[152:155], v[66:69], v[240:255]
	ds_write_b32 v231, v214 offset:536
	ds_write_b32 v232, v214 offset:560
	s_waitcnt lgkmcnt(5)
	v_mfma_f32_32x32x16_f16 v[240:255], v[148:151], v[48:51], v[240:255]
	ds_read_b128 v[66:69], v205 offset:51744
	ds_read_b128 v[44:47], v207 offset:51744
	s_waitcnt lgkmcnt(6)
	v_mfma_f32_32x32x16_f16 v[240:255], v[144:147], v[40:43], v[240:255]
	s_waitcnt lgkmcnt(5)
	v_mfma_f32_32x32x16_f16 v[88:103], v[132:135], v[52:55], v[88:103]
	ds_read_b128 v[52:55], v205 offset:52800
	ds_read_b128 v[48:51], v207 offset:52800
	s_waitcnt lgkmcnt(6)
	v_mfma_f32_32x32x16_f16 v[88:103], v[108:111], v[82:85], v[88:103]
	s_and_saveexec_b64 s[2:3], s[0:1]
	s_cbranch_execz .LBB2_124
	ds_write_b128 v210, v[28:31] offset:16
	ds_write_b32 v233, v71 offset:548
	ds_write_b32 v234, v71 offset:536
	ds_write_b32 v235, v71 offset:560
.LBB2_124:
	s_or_b64 exec, exec, s[2:3]
	s_waitcnt lgkmcnt(3)
	v_mfma_f32_32x32x16_f16 v[88:103], v[128:131], v[66:69], v[88:103]
	ds_read_b128 v[40:43], v205 offset:53856
	ds_read_b128 v[28:31], v207 offset:53856
	v_mfma_f32_32x32x16_f16 v[240:255], v[132:135], v[66:69], v[240:255]
	s_waitcnt lgkmcnt(4)
	v_mfma_f32_32x32x16_f16 v[88:103], v[124:127], v[44:47], v[88:103]
	v_mfma_f32_32x32x16_f16 v[240:255], v[108:111], v[44:47], v[240:255]
	s_waitcnt lgkmcnt(3)
	v_mfma_f32_32x32x16_f16 v[88:103], v[116:119], v[52:55], v[88:103]
	v_mfma_f32_32x32x16_f16 v[240:255], v[128:131], v[52:55], v[240:255]
	s_waitcnt lgkmcnt(2)
	v_mfma_f32_32x32x16_f16 v[88:103], v[112:115], v[48:51], v[88:103]
	v_mfma_f32_32x32x16_f16 v[240:255], v[124:127], v[48:51], v[240:255]
	s_and_saveexec_b64 s[2:3], s[8:9]
	s_cbranch_execz .LBB2_129
	ds_write_b128 v211, v[24:27] offset:16
	ds_write_b32 v236, v87 offset:548
	ds_write_b32 v237, v87 offset:536
	ds_write_b32 v238, v87 offset:560

	.amdhsa_kernel _Z7k2_mfmaPK15HIP_vector_typeIjLj4EEPKjS2_PKfPS0_Pj
		.amdhsa_group_segment_fixed_size 0
		.amdhsa_private_segment_fixed_size 0
		.amdhsa_kernarg_size 304
		.amdhsa_user_sgpr_count 2
		.amdhsa_user_sgpr_dispatch_ptr 0
		.amdhsa_user_sgpr_queue_ptr 0
		.amdhsa_user_sgpr_kernarg_segment_ptr 1
		.amdhsa_user_sgpr_dispatch_id 0
		.amdhsa_user_sgpr_kernarg_preload_length 0
		.amdhsa_user_sgpr_kernarg_preload_offset 0
		.amdhsa_user_sgpr_private_segment_size 0
		.amdhsa_uses_dynamic_stack 0
		.amdhsa_enable_private_segment 0
		.amdhsa_system_sgpr_workgroup_id_x 1
		.amdhsa_system_sgpr_workgroup_id_y 0
		.amdhsa_system_sgpr_workgroup_id_z 0
		.amdhsa_system_sgpr_workgroup_info 0
		.amdhsa_system_vgpr_workitem_id 0
		.amdhsa_next_free_vgpr 256
		.amdhsa_next_free_sgpr 50
		.amdhsa_accum_offset 256
		.amdhsa_reserve_vcc 1
		.amdhsa_float_round_mode_32 0
		.amdhsa_float_round_mode_16_64 0
		.amdhsa_float_denorm_mode_32 3
		.amdhsa_float_denorm_mode_16_64 3
		.amdhsa_dx10_clamp 1
		.amdhsa_ieee_mode 1
		.amdhsa_fp16_overflow 0
		.amdhsa_tg_split 0
		.amdhsa_exception_fp_ieee_invalid_op 0
		.amdhsa_exception_fp_denorm_src 0
		.amdhsa_exception_fp_ieee_div_zero 0
		.amdhsa_exception_fp_ieee_overflow 0
		.amdhsa_exception_fp_ieee_underflow 0
		.amdhsa_exception_fp_ieee_inexact 0
		.amdhsa_exception_int_div_zero 0
	.end_amdhsa_kernel

.LBB6_525:
	s_or_b64 exec, exec, s[10:11]
	v_mov_b32_e32 v33, v24
	v_mov_b32_e32 v24, v25
	v_mov_b32_e32 v25, v26
	v_pk_add_f32 v[184:185], v[68:69], v[24:25]
	v_mov_b32_e32 v24, v82
	v_mov_b32_e32 v25, v70
	v_mov_b32_e32 v26, v55
	v_pk_add_f32 v[180:181], v[24:25], v[26:27]
	v_mov_b32_e32 v24, v83
	v_mov_b32_e32 v25, v84
	v_mov_b32_e32 v32, v23
	v_pk_add_f32 v[186:187], v[24:25], v[56:57]
	v_mov_b32_e32 v24, v85
	v_mov_b32_e32 v25, v86
	v_pk_add_f32 v[182:183], v[66:67], v[32:33]
	v_pk_add_f32 v[188:189], v[24:25], v[58:59]
	s_waitcnt lgkmcnt(1)
	v_mfma_f32_32x32x16_f16 v[2:17], v[116:119], v[60:63], v[2:17]
	s_waitcnt lgkmcnt(0)
	v_mfma_f32_32x32x16_f16 v[2:17], v[112:115], v[28:31], v[2:17]
	s_add_i32 s3, s3, s33
	s_bfe_u32 s3, s3, 0x30003
	s_lshl_b32 s10, s3, 17
	s_lshl_b32 s2, s2, 9
	s_add_i32 s10, s40, s10
	s_and_b32 s2, s2, 0x7000
	s_add_i32 s2, s2, s10
	s_nop 4
	v_lshl_add_u32 v17, v200, 15, s2
	v_add_lshl_u32 v23, v201, v191, 10
	s_movk_i32 s10, 0xfc80
	v_add3_u32 v193, v17, v23, s10
	v_lshl_add_u32 v17, v198, 15, s2
	v_add_lshl_u32 v23, v199, v197, 10
	s_mov_b32 s10, 0xffff7c80
	v_add3_u32 v216, v17, v23, s10
	v_lshl_add_u32 v17, v195, 15, s2
	v_add_lshl_u32 v23, v196, v191, 10
	v_add3_u32 v217, v17, v23, s10
	s_lshl_b32 s2, s3, 7
	v_lshlrev_b32_e32 v17, 5, v194
	v_or3_b32 v17, v190, s2, v17
	v_add_u32_e32 v17, s41, v17
	v_add_lshl_u32 v17, v17, v202, 10
	v_add3_u32 v32, s40, v17, v206
	v_mov_b32_e32 v33, 0
	v_add_u32_e32 v17, 32, v32
	v_lshlrev_b64 v[194:195], 4, v[32:33]
	v_lshl_add_u64 v[24:25], v[32:33], 2, s[18:19]
	s_mov_b64 s[10:11], 0x100
	v_lshlrev_b32_e32 v32, 2, v17
	s_mov_b32 s33, 2
	v_lshl_add_u64 v[196:197], v[24:25], 0, s[10:11]
	v_lshl_add_u64 v[198:199], s[18:19], 0, v[32:33]
	v_lshlrev_b32_e32 v200, 4, v17
	v_mov_b32_e32 v201, v33
	v_mbcnt_lo_u32_b32 v24, -1, 0
	v_mbcnt_hi_u32_b32 v24, -1, v24
	v_and_b32_e32 v24, 31, v24
	v_cmp_eq_u32_e64 s[70:71], 0, v24
	v_cmp_eq_u32_e64 s[72:73], 31, v24
	v_mul_u32_u24_e32 v25, 11, v24
	v_lshrrev_b32_e32 v25, 5, v25
	v_mul_u32_u24_e32 v25, 3, v25
	v_sub_u32_e32 v24, v24, v25
	v_mul_u32_u24_e32 v26, 12, v24
	v_cndmask_b32_e64 v26, v26, 12, s[70:71]
	v_add_u32_e32 v25, 2, v24
	v_mul_u32_u24_e32 v27, 11, v25
	v_lshrrev_b32_e32 v27, 5, v27
	v_mul_u32_u24_e32 v27, 3, v27
	v_sub_u32_e32 v25, v25, v27
	v_mul_u32_u24_e32 v25, 12, v25
	v_add_u32_e32 v25, -12, v25
	v_add_u32_e32 v24, 1, v24
	v_mul_u32_u24_e32 v27, 11, v24
	v_lshrrev_b32_e32 v27, 5, v27
	v_mul_u32_u24_e32 v27, 3, v27
	v_sub_u32_e32 v24, v24, v27
	v_mul_u32_u24_e32 v24, 12, v24
	v_add_u32_e32 v24, 0xffffffe8, v24
	v_cndmask_b32_e64 v24, v24, -12, s[72:73]
	v_add_u32_e32 v230, v212, v25
	v_add_u32_e32 v231, v212, v26
	v_add_u32_e32 v232, v212, v24
	v_add_u32_e32 v233, v214, v25
	v_add_u32_e32 v234, v214, v26
	v_add_u32_e32 v235, v214, v24
	v_add_u32_e32 v236, v215, v25
	v_add_u32_e32 v237, v215, v26
	v_add_u32_e32 v238, v215, v24
	s_barrier

.LBB6_532:
	s_or_b64 exec, exec, s[34:35]
	v_mfma_f32_32x32x16_f16 v[56:71], v[164:167], v[72:75], v[56:71]
	ds_read_b128 v[218:221], v209 offset:3168
	ds_read_b128 v[222:225], v211 offset:3168
	v_mfma_f32_32x32x16_f16 v[72:87], v[176:179], v[72:75], 0
	s_waitcnt lgkmcnt(3)
	v_mfma_f32_32x32x16_f16 v[56:71], v[160:163], v[100:103], v[56:71]
	v_mfma_f32_32x32x16_f16 v[72:87], v[172:175], v[100:103], v[72:87]
	v_mfma_f32_32x32x16_f16 v[56:71], v[168:171], v[96:99], v[56:71]
	v_mfma_f32_32x32x16_f16 v[72:87], v[164:167], v[96:99], v[72:87]
	ds_read_b128 v[96:99], v209 offset:6336
	ds_read_b128 v[100:103], v211 offset:6336
	s_waitcnt lgkmcnt(4)
	v_mfma_f32_32x32x16_f16 v[56:71], v[156:159], v[92:95], v[56:71]
	v_mfma_f32_32x32x16_f16 v[72:87], v[160:163], v[92:95], v[72:87]
	v_add_f32_e32 v14, v187, v14
	v_add_f32_e32 v15, v188, v15
	s_waitcnt lgkmcnt(3)
	v_mfma_f32_32x32x16_f16 v[72:87], v[168:171], v[218:221], v[72:87]
	v_add_f32_e32 v12, v180, v12
	v_add_f32_e32 v13, v186, v13
	v_max_f32_e32 v14, 0, v14
	v_max_f32_e32 v15, 0, v15
	v_max_f32_e32 v12, 0, v12
	v_max_f32_e32 v13, 0, v13
	v_cvt_pk_f16_f32 v15, v14, v15
	v_cvt_pk_f16_f32 v14, v12, v13
	v_add_f32_e32 v12, v189, v16
	v_max_f32_e32 v16, 0, v12
	v_add_f32_e32 v12, v184, v46
	v_add_f32_e32 v13, v185, v47
	v_max_f32_e32 v12, 0, v12
	v_max_f32_e32 v13, 0, v13
	s_waitcnt lgkmcnt(2)
	v_mfma_f32_32x32x16_f16 v[72:87], v[156:159], v[222:225], v[72:87]
	v_cvt_pk_f16_f32 v13, v12, v13
	v_add_f32_e32 v12, v182, v44
	v_add_f32_e32 v44, v183, v45
	v_max_f32_e32 v12, 0, v12
	v_max_f32_e32 v44, 0, v44
	ds_read_b128 v[92:95], v209 offset:7392
	ds_read_b128 v[226:229], v211 offset:7392
	v_cvt_pk_f16_f32 v12, v12, v44
	v_add_f32_e32 v44, v181, v48
	v_max_f32_e32 v46, 0, v44
	v_permlane32_swap_b32_e32 v12, v14
	v_permlane32_swap_b32_e32 v13, v15
	v_permlane32_swap_b32_e32 v46, v16
	v_lshl_add_u64 v[44:45], s[20:21], 0, v[200:201]
	global_store_dwordx4 v[44:45], v[12:15], off sc1
	s_nop 1
	v_cvt_pk_f16_f32 v12, v46, v16
	global_store_dword v[198:199], v12, off sc1
	s_waitcnt lgkmcnt(3)
	v_mfma_f32_32x32x16_f16 v[56:71], v[132:135], v[96:99], v[56:71]
	ds_read_b128 v[96:99], v209 offset:8448
	ds_read_b128 v[180:183], v211 offset:8448
	s_waitcnt lgkmcnt(4)
	v_mfma_f32_32x32x16_f16 v[56:71], v[140:143], v[100:103], v[56:71]
	s_waitcnt lgkmcnt(3)
	v_mfma_f32_32x32x16_f16 v[56:71], v[120:123], v[92:95], v[56:71]
	ds_read_b128 v[12:15], v209 offset:9504
	ds_read_b128 v[44:47], v211 offset:9504
	v_mfma_f32_32x32x16_f16 v[72:87], v[132:135], v[92:95], v[72:87]
	s_waitcnt lgkmcnt(4)
	v_mfma_f32_32x32x16_f16 v[56:71], v[152:155], v[226:229], v[56:71]
	v_mfma_f32_32x32x16_f16 v[72:87], v[140:143], v[226:229], v[72:87]
	s_waitcnt lgkmcnt(3)
	v_mfma_f32_32x32x16_f16 v[56:71], v[148:151], v[96:99], v[56:71]
	v_mfma_f32_32x32x16_f16 v[72:87], v[120:123], v[96:99], v[72:87]
	ds_read_b128 v[100:103], v209 offset:12672
	ds_read_b128 v[96:99], v211 offset:12672
	s_waitcnt vmcnt(3)
	ds_write_b128 v212, v[88:91] offset:38032
	s_waitcnt vmcnt(2)
	ds_write_b32 v230, v49 offset:38564
	s_waitcnt lgkmcnt(6)
	v_mfma_f32_32x32x16_f16 v[56:71], v[144:147], v[180:183], v[56:71]
	v_mfma_f32_32x32x16_f16 v[72:87], v[152:155], v[180:183], v[72:87]
	ds_write_b32 v231, v49 offset:38552
	ds_write_b32 v232, v49 offset:38576
	s_waitcnt lgkmcnt(5)
	v_mfma_f32_32x32x16_f16 v[72:87], v[148:151], v[12:15], v[72:87]
	ds_read_b128 v[92:95], v209 offset:13728
	ds_read_b128 v[12:15], v211 offset:13728
	s_waitcnt lgkmcnt(6)
	v_mfma_f32_32x32x16_f16 v[72:87], v[144:147], v[44:47], v[72:87]
	s_waitcnt lgkmcnt(5)
	v_mfma_f32_32x32x16_f16 v[56:71], v[136:139], v[100:103], v[56:71]
	ds_read_b128 v[88:91], v209 offset:14784
	ds_read_b128 v[44:47], v211 offset:14784
	s_waitcnt lgkmcnt(6)
	v_mfma_f32_32x32x16_f16 v[56:71], v[108:111], v[96:99], v[56:71]
	s_and_saveexec_b64 s[34:35], s[0:1]
	s_cbranch_execz .LBB6_541
	ds_write_b128 v214, v[28:31] offset:38032
	ds_write_b32 v233, v23 offset:38564
	ds_write_b32 v234, v23 offset:38552
	ds_write_b32 v235, v23 offset:38576
.LBB6_541:
	s_or_b64 exec, exec, s[34:35]
	s_waitcnt lgkmcnt(3)
	v_mfma_f32_32x32x16_f16 v[56:71], v[128:131], v[92:95], v[56:71]
	v_mfma_f32_32x32x16_f16 v[72:87], v[136:139], v[92:95], v[72:87]
	ds_read_b128 v[92:95], v209 offset:15840
	ds_read_b128 v[28:31], v211 offset:15840
	s_waitcnt lgkmcnt(4)
	v_mfma_f32_32x32x16_f16 v[56:71], v[124:127], v[12:15], v[56:71]
	v_mfma_f32_32x32x16_f16 v[72:87], v[108:111], v[12:15], v[72:87]
	s_waitcnt lgkmcnt(3)
	s_and_saveexec_b64 s[34:35], s[8:9]
	s_cbranch_execz .LBB6_546
	ds_write_b128 v215, v[24:27] offset:38032
	ds_write_b32 v236, v17 offset:38564
	ds_write_b32 v237, v17 offset:38552
	ds_write_b32 v238, v17 offset:38576
.LBB6_546:
	s_or_b64 exec, exec, s[34:35]
	s_waitcnt lgkmcnt(0)
	s_barrier
	ds_read_b128 v[24:27], v209 offset:38016
	ds_read_b128 v[12:15], v209 offset:39072
	v_mfma_f32_32x32x16_f16 v[56:71], v[116:119], v[88:91], v[56:71]
	v_mfma_f32_32x32x16_f16 v[72:87], v[128:131], v[88:91], v[72:87]
	v_mfma_f32_32x32x16_f16 v[56:71], v[112:115], v[44:47], v[56:71]
	v_mfma_f32_32x32x16_f16 v[72:87], v[124:127], v[44:47], v[72:87]
	v_mfma_f32_32x32x16_f16 v[72:87], v[116:119], v[92:95], v[72:87]
	v_mfma_f32_32x32x16_f16 v[72:87], v[112:115], v[28:31], v[72:87]
	s_waitcnt lgkmcnt(1)
	v_mfma_f32_32x32x16_f16 v[88:103], v[176:179], v[24:27], 0
	ds_read_b128 v[24:27], v211 offset:38016
	ds_read_b128 v[184:187], v209 offset:40128
	ds_read_b128 v[188:191], v211 offset:39072
	ds_read_b128 v[180:183], v211 offset:40128
	v_mov_b32_e32 v44, 0
	v_mov_b32_e32 v45, 0
	v_mov_b32_e32 v46, 0
	v_mov_b32_e32 v47, 0
	v_mov_b32_e32 v71, 0
	s_nop 1
	v_mov_b32_e32 v87, 0
	s_waitcnt lgkmcnt(3)
	v_mfma_f32_32x32x16_f16 v[88:103], v[172:175], v[24:27], v[88:103]
	s_and_saveexec_b64 s[34:35], s[28:29]
	s_cbranch_execz .LBB6_548
	v_lshl_add_u64 v[16:17], v[32:33], 4, s[12:13]
	global_load_dwordx4 v[44:47], v[16:17], off offset:512
	v_lshl_add_u64 v[16:17], v[32:33], 2, s[14:15]
	global_load_dword v87, v[16:17], off offset:128

.LBB6_552:
	s_or_b64 exec, exec, s[28:29]
	v_add_f32_e32 v39, v18, v39
	v_add_f32_e32 v202, v19, v40
	v_add_f32_e32 v203, v20, v41
	v_add_f32_e32 v204, v21, v42
	v_add_f32_e32 v205, v22, v43
	v_add_f32_e32 v7, v50, v7
	v_add_f32_e32 v218, v51, v8
	v_add_f32_e32 v219, v52, v9
	v_add_f32_e32 v220, v53, v10
	v_add_f32_e32 v221, v54, v11
	v_mfma_f32_32x32x16_f16 v[88:103], v[164:167], v[12:15], v[88:103]
	ds_read_b128 v[40:43], v209 offset:41184
	ds_read_b128 v[48:51], v211 offset:41184
	v_mfma_f32_32x32x16_f16 v[240:255], v[176:179], v[12:15], 0
	s_waitcnt lgkmcnt(3)
	v_mfma_f32_32x32x16_f16 v[88:103], v[160:163], v[188:191], v[88:103]
	v_mfma_f32_32x32x16_f16 v[240:255], v[172:175], v[188:191], v[240:255]
	v_mfma_f32_32x32x16_f16 v[88:103], v[168:171], v[184:187], v[88:103]
	v_mfma_f32_32x32x16_f16 v[240:255], v[164:167], v[184:187], v[240:255]
	ds_read_b128 v[52:55], v209 offset:44352
	ds_read_b128 v[184:187], v211 offset:44352
	s_waitcnt lgkmcnt(4)
	v_mfma_f32_32x32x16_f16 v[88:103], v[156:159], v[180:183], v[88:103]
	v_mfma_f32_32x32x16_f16 v[240:255], v[160:163], v[180:183], v[240:255]
	v_add_f32_e32 v84, v219, v84
	v_add_f32_e32 v85, v220, v85
	s_waitcnt lgkmcnt(3)
	v_mfma_f32_32x32x16_f16 v[240:255], v[168:171], v[40:43], v[240:255]
	v_add_f32_e32 v40, 0, v85
	v_max_f32_e32 v84, 0, v84
	v_max_f32_e32 v40, 0, v40
	v_cvt_pk_f16_f32 v43, v84, v40
	v_add_f32_e32 v7, v7, v82
	v_add_f32_e32 v40, v218, v83
	v_max_f32_e32 v7, 0, v7
	v_max_f32_e32 v40, 0, v40
	v_cvt_pk_f16_f32 v42, v7, v40
	v_add_f32_e32 v40, v203, v68
	v_add_f32_e32 v41, v204, v69
	v_max_f32_e32 v40, 0, v40
	v_max_f32_e32 v41, 0, v41
	s_waitcnt lgkmcnt(2)
	v_mfma_f32_32x32x16_f16 v[240:255], v[156:159], v[48:51], v[240:255]
	v_cvt_pk_f16_f32 v41, v40, v41
	v_add_f32_e32 v39, v39, v66
	v_add_f32_e32 v40, v202, v67
	v_max_f32_e32 v39, 0, v39
	v_max_f32_e32 v40, 0, v40
	ds_read_b128 v[180:183], v209 offset:45408
	ds_read_b128 v[188:191], v211 offset:45408
	v_add_f32_e32 v7, v221, v86
	v_cvt_pk_f16_f32 v40, v39, v40
	v_add_f32_e32 v39, v205, v70
	v_max_f32_e32 v7, 0, v7
	v_max_f32_e32 v39, 0, v39
	s_nop 1
	v_permlane32_swap_b32_e32 v39, v7
	v_permlane32_swap_b32_e32 v40, v42
	v_permlane32_swap_b32_e32 v41, v43
	v_lshl_add_u64 v[48:49], s[20:21], 0, v[194:195]
	v_cvt_pk_f16_f32 v7, v39, v7
	global_store_dwordx4 v[48:49], v[40:43], off offset:1024 sc1
	global_store_dword v[196:197], v7, off sc1
	s_waitcnt lgkmcnt(3)
	v_mfma_f32_32x32x16_f16 v[88:103], v[132:135], v[52:55], v[88:103]
	ds_read_b128 v[52:55], v209 offset:46464
	ds_read_b128 v[66:69], v211 offset:46464
	s_waitcnt lgkmcnt(4)
	v_mfma_f32_32x32x16_f16 v[88:103], v[140:143], v[184:187], v[88:103]
	s_waitcnt lgkmcnt(3)
	v_mfma_f32_32x32x16_f16 v[88:103], v[120:123], v[180:183], v[88:103]
	ds_read_b128 v[48:51], v209 offset:47520
	ds_read_b128 v[40:43], v211 offset:47520
	v_mfma_f32_32x32x16_f16 v[240:255], v[132:135], v[180:183], v[240:255]
	s_waitcnt lgkmcnt(4)
	v_mfma_f32_32x32x16_f16 v[88:103], v[152:155], v[188:191], v[88:103]
	v_mfma_f32_32x32x16_f16 v[240:255], v[140:143], v[188:191], v[240:255]
	s_waitcnt lgkmcnt(3)
	v_mfma_f32_32x32x16_f16 v[88:103], v[148:151], v[52:55], v[88:103]
	v_mfma_f32_32x32x16_f16 v[240:255], v[120:123], v[52:55], v[240:255]
	ds_read_b128 v[52:55], v209 offset:50688
	ds_read_b128 v[82:85], v211 offset:50688
	s_waitcnt vmcnt(3)
	ds_write_b128 v212, v[44:47] offset:16
	s_waitcnt vmcnt(2)
	ds_write_b32 v230, v87 offset:548
	s_waitcnt lgkmcnt(6)
	v_mfma_f32_32x32x16_f16 v[88:103], v[144:147], v[66:69], v[88:103]
	v_mfma_f32_32x32x16_f16 v[240:255], v[152:155], v[66:69], v[240:255]
	ds_write_b32 v231, v87 offset:536
	ds_write_b32 v232, v87 offset:560
	s_waitcnt lgkmcnt(5)
	v_mfma_f32_32x32x16_f16 v[240:255], v[148:151], v[48:51], v[240:255]
	ds_read_b128 v[66:69], v209 offset:51744
	ds_read_b128 v[44:47], v211 offset:51744
	s_waitcnt lgkmcnt(6)
	v_mfma_f32_32x32x16_f16 v[240:255], v[144:147], v[40:43], v[240:255]
	s_waitcnt lgkmcnt(5)
	v_mfma_f32_32x32x16_f16 v[88:103], v[136:139], v[52:55], v[88:103]
	ds_read_b128 v[52:55], v209 offset:52800
	ds_read_b128 v[48:51], v211 offset:52800
	s_waitcnt lgkmcnt(6)
	v_mfma_f32_32x32x16_f16 v[88:103], v[108:111], v[82:85], v[88:103]
	s_and_saveexec_b64 s[2:3], s[0:1]
	s_cbranch_execz .LBB6_561
	ds_write_b128 v214, v[28:31] offset:16
	ds_write_b32 v233, v71 offset:548
	ds_write_b32 v234, v71 offset:536
	ds_write_b32 v235, v71 offset:560
.LBB6_561:
	s_or_b64 exec, exec, s[2:3]
	s_waitcnt lgkmcnt(3)
	v_mfma_f32_32x32x16_f16 v[88:103], v[128:131], v[66:69], v[88:103]
	ds_read_b128 v[40:43], v209 offset:53856
	ds_read_b128 v[28:31], v211 offset:53856
	v_mfma_f32_32x32x16_f16 v[240:255], v[136:139], v[66:69], v[240:255]
	s_waitcnt lgkmcnt(4)
	v_mfma_f32_32x32x16_f16 v[88:103], v[124:127], v[44:47], v[88:103]
	v_mfma_f32_32x32x16_f16 v[240:255], v[108:111], v[44:47], v[240:255]
	s_waitcnt lgkmcnt(3)
	v_mfma_f32_32x32x16_f16 v[88:103], v[116:119], v[52:55], v[88:103]
	v_mfma_f32_32x32x16_f16 v[240:255], v[128:131], v[52:55], v[240:255]
	s_waitcnt lgkmcnt(2)
	v_mfma_f32_32x32x16_f16 v[88:103], v[112:115], v[48:51], v[88:103]
	v_mfma_f32_32x32x16_f16 v[240:255], v[124:127], v[48:51], v[240:255]
	s_and_saveexec_b64 s[2:3], s[8:9]
	s_cbranch_execz .LBB6_566
	ds_write_b128 v215, v[24:27] offset:16
	ds_write_b32 v236, v32 offset:548
	ds_write_b32 v237, v32 offset:536
	ds_write_b32 v238, v32 offset:560

	.amdhsa_kernel _Z8k23_mfmaPK15HIP_vector_typeIjLj4EEPKjS2_PKfPS0_PjS2_S4_S2_S6_Pf
		.amdhsa_group_segment_fixed_size 0
		.amdhsa_private_segment_fixed_size 0
		.amdhsa_kernarg_size 88
		.amdhsa_user_sgpr_count 2
		.amdhsa_user_sgpr_dispatch_ptr 0
		.amdhsa_user_sgpr_queue_ptr 0
		.amdhsa_user_sgpr_kernarg_segment_ptr 1
		.amdhsa_user_sgpr_dispatch_id 0
		.amdhsa_user_sgpr_kernarg_preload_length 0
		.amdhsa_user_sgpr_kernarg_preload_offset 0
		.amdhsa_user_sgpr_private_segment_size 0
		.amdhsa_uses_dynamic_stack 0
		.amdhsa_enable_private_segment 0
		.amdhsa_system_sgpr_workgroup_id_x 1
		.amdhsa_system_sgpr_workgroup_id_y 0
		.amdhsa_system_sgpr_workgroup_id_z 0
		.amdhsa_system_sgpr_workgroup_info 0
		.amdhsa_system_vgpr_workitem_id 0
		.amdhsa_next_free_vgpr 256
		.amdhsa_next_free_sgpr 74
		.amdhsa_accum_offset 256
		.amdhsa_reserve_vcc 1
		.amdhsa_float_round_mode_32 0
		.amdhsa_float_round_mode_16_64 0
		.amdhsa_float_denorm_mode_32 3
		.amdhsa_float_denorm_mode_16_64 3
		.amdhsa_dx10_clamp 1
		.amdhsa_ieee_mode 1
		.amdhsa_fp16_overflow 0
		.amdhsa_tg_split 0
		.amdhsa_exception_fp_ieee_invalid_op 0
		.amdhsa_exception_fp_denorm_src 0
		.amdhsa_exception_fp_ieee_div_zero 0
		.amdhsa_exception_fp_ieee_overflow 0
		.amdhsa_exception_fp_ieee_underflow 0
		.amdhsa_exception_fp_ieee_inexact 0
		.amdhsa_exception_int_div_zero 0
	.end_amdhsa_kernel

amdhsa.kernels:
  - .agpr_count:     0
    .args:
      - .actual_access:  read_only
        .address_space:  global
        .offset:         0
        .size:           8
        .value_kind:     global_buffer
      - .actual_access:  read_only
        .address_space:  global
        .offset:         8
        .size:           8
        .value_kind:     global_buffer
      - .actual_access:  read_only
        .address_space:  global
        .offset:         16
        .size:           8
        .value_kind:     global_buffer
      - .actual_access:  write_only
        .address_space:  global
        .offset:         24
        .size:           8
        .value_kind:     global_buffer
      - .actual_access:  write_only
        .address_space:  global
        .offset:         32
        .size:           8
        .value_kind:     global_buffer
    .group_segment_fixed_size: 6520
    .kernarg_segment_align: 8
    .kernarg_segment_size: 40
    .language:       OpenCL C
    .language_version:
      - 2
      - 0
    .max_flat_workgroup_size: 256
    .name:           _Z8k1_naivePKfS0_S0_P15HIP_vector_typeIjLj4EEPj
    .private_segment_fixed_size: 0
    .sgpr_count:     30
    .sgpr_spill_count: 0
    .symbol:         _Z8k1_naivePKfS0_S0_P15HIP_vector_typeIjLj4EEPj.kd
    .uniform_work_group_size: 1
    .uses_dynamic_stack: false
    .vgpr_count:     40
    .vgpr_spill_count: 0
    .wavefront_size: 64
  - .agpr_count:     0
    .args:
      - .actual_access:  read_only
        .address_space:  global
        .offset:         0
        .size:           8
        .value_kind:     global_buffer
      - .actual_access:  read_only
        .address_space:  global
        .offset:         8
        .size:           8
        .value_kind:     global_buffer
      - .actual_access:  read_only
        .address_space:  global
        .offset:         16
        .size:           8
        .value_kind:     global_buffer
      - .actual_access:  read_only
        .address_space:  global
        .offset:         24
        .size:           8
        .value_kind:     global_buffer
      - .actual_access:  write_only
        .address_space:  global
        .offset:         32
        .size:           8
        .value_kind:     global_buffer
      - .actual_access:  write_only
        .address_space:  global
        .offset:         40
        .size:           8
        .value_kind:     global_buffer
      - .offset:         48
        .size:           4
        .value_kind:     by_value
    .group_segment_fixed_size: 32448
    .kernarg_segment_align: 8
    .kernarg_segment_size: 52
    .language:       OpenCL C
    .language_version:
      - 2
      - 0
    .max_flat_workgroup_size: 256
    .name:           _Z8k2_naivePK15HIP_vector_typeIjLj4EEPKjPKfS6_PS0_Pji
    .private_segment_fixed_size: 0
    .sgpr_count:     30
    .sgpr_spill_count: 0
    .symbol:         _Z8k2_naivePK15HIP_vector_typeIjLj4EEPKjPKfS6_PS0_Pji.kd
    .uniform_work_group_size: 1
    .uses_dynamic_stack: false
    .vgpr_count:     102
    .vgpr_spill_count: 0
    .wavefront_size: 64
  - .agpr_count:     0
    .args:
      - .actual_access:  read_only
        .address_space:  global
        .offset:         0
        .size:           8
        .value_kind:     global_buffer
      - .actual_access:  read_only
        .address_space:  global
        .offset:         8
        .size:           8
        .value_kind:     global_buffer
      - .actual_access:  read_only
        .address_space:  global
        .offset:         16
        .size:           8
        .value_kind:     global_buffer
      - .actual_access:  read_only
        .address_space:  global
        .offset:         24
        .size:           8
        .value_kind:     global_buffer
      - .actual_access:  write_only
        .address_space:  global
        .offset:         32
        .size:           8
        .value_kind:     global_buffer
      - .actual_access:  write_only
        .address_space:  global
        .offset:         40
        .size:           8
        .value_kind:     global_buffer
      - .offset:         48
        .size:           4
        .value_kind:     hidden_block_count_x
      - .offset:         52
        .size:           4
        .value_kind:     hidden_block_count_y
      - .offset:         56
        .size:           4
        .value_kind:     hidden_block_count_z
      - .offset:         60
        .size:           2
        .value_kind:     hidden_group_size_x
      - .offset:         62
        .size:           2
        .value_kind:     hidden_group_size_y
      - .offset:         64
        .size:           2
        .value_kind:     hidden_group_size_z
      - .offset:         66
        .size:           2
        .value_kind:     hidden_remainder_x
      - .offset:         68
        .size:           2
        .value_kind:     hidden_remainder_y
      - .offset:         70
        .size:           2
        .value_kind:     hidden_remainder_z
      - .offset:         88
        .size:           8
        .value_kind:     hidden_global_offset_x
      - .offset:         96
        .size:           8
        .value_kind:     hidden_global_offset_y
      - .offset:         104
        .size:           8
        .value_kind:     hidden_global_offset_z
      - .offset:         112
        .size:           2
        .value_kind:     hidden_grid_dims
      - .offset:         168
        .size:           4
        .value_kind:     hidden_dynamic_lds_size
    .group_segment_fixed_size: 0
    .kernarg_segment_align: 8
    .kernarg_segment_size: 304
    .language:       OpenCL C
    .language_version:
      - 2
      - 0
    .max_flat_workgroup_size: 512
    .name:           _Z7k2_mfmaPK15HIP_vector_typeIjLj4EEPKjS2_PKfPS0_Pj
    .private_segment_fixed_size: 0
    .sgpr_count:     56
    .sgpr_spill_count: 0
    .symbol:         _Z7k2_mfmaPK15HIP_vector_typeIjLj4EEPKjS2_PKfPS0_Pj.kd
    .uniform_work_group_size: 1
    .uses_dynamic_stack: false
    .vgpr_count:     256
    .vgpr_spill_count: 0
    .wavefront_size: 64
  - .agpr_count:     0
    .args:
      - .actual_access:  read_only
        .address_space:  global
        .offset:         0
        .size:           8
        .value_kind:     global_buffer
      - .actual_access:  write_only
        .address_space:  global
        .offset:         8
        .size:           8
        .value_kind:     global_buffer
      - .offset:         16
        .size:           4
        .value_kind:     hidden_block_count_x
      - .offset:         20
        .size:           4
        .value_kind:     hidden_block_count_y
      - .offset:         24
        .size:           4
        .value_kind:     hidden_block_count_z
      - .offset:         28
        .size:           2
        .value_kind:     hidden_group_size_x
      - .offset:         30
        .size:           2
        .value_kind:     hidden_group_size_y
      - .offset:         32
        .size:           2
        .value_kind:     hidden_group_size_z
      - .offset:         34
        .size:           2
        .value_kind:     hidden_remainder_x
      - .offset:         36
        .size:           2
        .value_kind:     hidden_remainder_y
      - .offset:         38
        .size:           2
        .value_kind:     hidden_remainder_z
      - .offset:         56
        .size:           8
        .value_kind:     hidden_global_offset_x
      - .offset:         64
        .size:           8
        .value_kind:     hidden_global_offset_y
      - .offset:         72
        .size:           8
        .value_kind:     hidden_global_offset_z
      - .offset:         80
        .size:           2
        .value_kind:     hidden_grid_dims
    .group_segment_fixed_size: 0
    .kernarg_segment_align: 8
    .kernarg_segment_size: 272
    .language:       OpenCL C
    .language_version:
      - 2
      - 0
    .max_flat_workgroup_size: 1024
    .name:           _Z7prep_w3PKfP15HIP_vector_typeIjLj4EE
    .private_segment_fixed_size: 0
    .sgpr_count:     18
    .sgpr_spill_count: 0
    .symbol:         _Z7prep_w3PKfP15HIP_vector_typeIjLj4EE.kd
    .uniform_work_group_size: 1
    .uses_dynamic_stack: false
    .vgpr_count:     13
    .vgpr_spill_count: 0
    .wavefront_size: 64
  - .agpr_count:     0
    .args:
      - .actual_access:  read_only
        .address_space:  global
        .offset:         0
        .size:           8
        .value_kind:     global_buffer
      - .actual_access:  read_only
        .address_space:  global
        .offset:         8
        .size:           8
        .value_kind:     global_buffer
      - .actual_access:  read_only
        .address_space:  global
        .offset:         16
        .size:           8
        .value_kind:     global_buffer
      - .actual_access:  read_only
        .address_space:  global
        .offset:         24
        .size:           8
        .value_kind:     global_buffer
      - .address_space:  global
        .offset:         32
        .size:           8
        .value_kind:     global_buffer
      - .offset:         40
        .size:           4
        .value_kind:     by_value
      - .offset:         48
        .size:           4
        .value_kind:     hidden_block_count_x
      - .offset:         52
        .size:           4
        .value_kind:     hidden_block_count_y
      - .offset:         56
        .size:           4
        .value_kind:     hidden_block_count_z
      - .offset:         60
        .size:           2
        .value_kind:     hidden_group_size_x
      - .offset:         62
        .size:           2
        .value_kind:     hidden_group_size_y
      - .offset:         64
        .size:           2
        .value_kind:     hidden_group_size_z
      - .offset:         66
        .size:           2
        .value_kind:     hidden_remainder_x
      - .offset:         68
        .size:           2
        .value_kind:     hidden_remainder_y
      - .offset:         70
        .size:           2
        .value_kind:     hidden_remainder_z
      - .offset:         88
        .size:           8
        .value_kind:     hidden_global_offset_x
      - .offset:         96
        .size:           8
        .value_kind:     hidden_global_offset_y
      - .offset:         104
        .size:           8
        .value_kind:     hidden_global_offset_z
      - .offset:         112
        .size:           2
        .value_kind:     hidden_grid_dims
    .group_segment_fixed_size: 25344
    .kernarg_segment_align: 8
    .kernarg_segment_size: 304
    .language:       OpenCL C
    .language_version:
      - 2
      - 0
    .max_flat_workgroup_size: 64
    .name:           _Z7k3_mfmaPK15HIP_vector_typeIjLj4EEPKjS2_PKfPfi
    .private_segment_fixed_size: 0
    .sgpr_count:     52
    .sgpr_spill_count: 0
    .symbol:         _Z7k3_mfmaPK15HIP_vector_typeIjLj4EEPKjS2_PKfPfi.kd
    .uniform_work_group_size: 1
    .uses_dynamic_stack: false
    .vgpr_count:     192
    .vgpr_spill_count: 0
    .wavefront_size: 64
  - .agpr_count:     0
    .args:
      - .actual_access:  read_only
        .address_space:  global
        .offset:         0
        .size:           8
        .value_kind:     global_buffer
      - .actual_access:  read_only
        .address_space:  global
        .offset:         8
        .size:           8
        .value_kind:     global_buffer
      - .actual_access:  read_only
        .address_space:  global
        .offset:         16
        .size:           8
        .value_kind:     global_buffer
      - .actual_access:  write_only
        .address_space:  global
        .offset:         24
        .size:           8
        .value_kind:     global_buffer
      - .actual_access:  write_only
        .address_space:  global
        .offset:         32
        .size:           8
        .value_kind:     global_buffer
      - .actual_access:  read_only
        .address_space:  global
        .offset:         40
        .size:           8
        .value_kind:     global_buffer
      - .actual_access:  read_only
        .address_space:  global
        .offset:         48
        .size:           8
        .value_kind:     global_buffer
      - .actual_access:  read_only
        .address_space:  global
        .offset:         56
        .size:           8
        .value_kind:     global_buffer
      - .actual_access:  write_only
        .address_space:  global
        .offset:         64
        .size:           8
        .value_kind:     global_buffer
      - .actual_access:  write_only
        .address_space:  global
        .offset:         72
        .size:           8
        .value_kind:     global_buffer
    .group_segment_fixed_size: 62848
    .kernarg_segment_align: 8
    .kernarg_segment_size: 80
    .language:       OpenCL C
    .language_version:
      - 2
      - 0
    .max_flat_workgroup_size: 256
    .name:           _Z7k1_mfmaPKfS0_S0_P15HIP_vector_typeIjLj4EEPjS0_S0_S0_S3_S3_
    .private_segment_fixed_size: 0
    .sgpr_count:     28
    .sgpr_spill_count: 0
    .symbol:         _Z7k1_mfmaPKfS0_S0_P15HIP_vector_typeIjLj4EEPjS0_S0_S0_S3_S3_.kd
    .uniform_work_group_size: 1
    .uses_dynamic_stack: false
    .vgpr_count:     170
    .vgpr_spill_count: 0
    .wavefront_size: 64
  - .agpr_count:     0
    .args:
      - .actual_access:  read_only
        .address_space:  global
        .offset:         0
        .size:           8
        .value_kind:     global_buffer
      - .actual_access:  read_only
        .address_space:  global
        .offset:         8
        .size:           8
        .value_kind:     global_buffer
      - .actual_access:  read_only
        .address_space:  global
        .offset:         16
        .size:           8
        .value_kind:     global_buffer
      - .actual_access:  read_only
        .address_space:  global
        .offset:         24
        .size:           8
        .value_kind:     global_buffer
      - .actual_access:  write_only
        .address_space:  global
        .offset:         32
        .size:           8
        .value_kind:     global_buffer
      - .actual_access:  write_only
        .address_space:  global
        .offset:         40
        .size:           8
        .value_kind:     global_buffer
      - .actual_access:  read_only
        .address_space:  global
        .offset:         48
        .size:           8
        .value_kind:     global_buffer
      - .actual_access:  read_only
        .address_space:  global
        .offset:         56
        .size:           8
        .value_kind:     global_buffer
      - .actual_access:  read_only
        .address_space:  global
        .offset:         64
        .size:           8
        .value_kind:     global_buffer
      - .actual_access:  read_only
        .address_space:  global
        .offset:         72
        .size:           8
        .value_kind:     global_buffer
      - .actual_access:  write_only
        .address_space:  global
        .offset:         80
        .size:           8
        .value_kind:     global_buffer
    .group_segment_fixed_size: 0
    .kernarg_segment_align: 8
    .kernarg_segment_size: 88
    .language:       OpenCL C
    .language_version:
      - 2
      - 0
    .max_flat_workgroup_size: 512
    .name:           _Z8k23_mfmaPK15HIP_vector_typeIjLj4EEPKjS2_PKfPS0_PjS2_S4_S2_S6_Pf
    .private_segment_fixed_size: 0
    .sgpr_count:     80
    .sgpr_spill_count: 0
    .symbol:         _Z8k23_mfmaPK15HIP_vector_typeIjLj4EEPKjS2_PKfPS0_PjS2_S4_S2_S6_Pf.kd
    .uniform_work_group_size: 1
    .uses_dynamic_stack: false
    .vgpr_count:     256
    .vgpr_spill_count: 0
    .wavefront_size: 64
  - .agpr_count:     0
    .args:
      - .actual_access:  read_only
        .address_space:  global
        .offset:         0
        .size:           8
        .value_kind:     global_buffer
      - .actual_access:  read_only
        .address_space:  global
        .offset:         8
        .size:           8
        .value_kind:     global_buffer
      - .actual_access:  read_only
        .address_space:  global
        .offset:         16
        .size:           8
        .value_kind:     global_buffer
      - .actual_access:  read_only
        .address_space:  global
        .offset:         24
        .size:           8
        .value_kind:     global_buffer
      - .address_space:  global
        .offset:         32
        .size:           8
        .value_kind:     global_buffer
      - .offset:         40
        .size:           4
        .value_kind:     by_value
    .group_segment_fixed_size: 3240
    .kernarg_segment_align: 8
    .kernarg_segment_size: 44
    .language:       OpenCL C
    .language_version:
      - 2
      - 0
    .max_flat_workgroup_size: 256
    .name:           _Z8k3_naivePK15HIP_vector_typeIjLj4EEPKjPKfS6_Pfi
    .private_segment_fixed_size: 0
    .sgpr_count:     28
    .sgpr_spill_count: 0
    .symbol:         _Z8k3_naivePK15HIP_vector_typeIjLj4EEPKjPKfS6_Pfi.kd
    .uniform_work_group_size: 1
    .uses_dynamic_stack: false
    .vgpr_count:     32
    .vgpr_spill_count: 0
    .wavefront_size: 64
  - .agpr_count:     0
    .args:
      - .actual_access:  read_only
        .address_space:  global
        .offset:         0
        .size:           8
        .value_kind:     global_buffer
      - .actual_access:  read_only
        .address_space:  global
        .offset:         8
        .size:           8
        .value_kind:     global_buffer
      - .actual_access:  read_only
        .address_space:  global
        .offset:         16
        .size:           8
        .value_kind:     global_buffer
      - .actual_access:  read_only
        .address_space:  global
        .offset:         24
        .size:           8
        .value_kind:     global_buffer
      - .address_space:  global
        .offset:         32
        .size:           8
        .value_kind:     global_buffer
      - .offset:         40
        .size:           4
        .value_kind:     hidden_block_count_x
      - .offset:         44
        .size:           4
        .value_kind:     hidden_block_count_y
      - .offset:         48
        .size:           4
        .value_kind:     hidden_block_count_z
      - .offset:         52
        .size:           2
        .value_kind:     hidden_group_size_x
      - .offset:         54
        .size:           2
        .value_kind:     hidden_group_size_y
      - .offset:         56
        .size:           2
        .value_kind:     hidden_group_size_z
      - .offset:         58
        .size:           2
        .value_kind:     hidden_remainder_x
      - .offset:         60
        .size:           2
        .value_kind:     hidden_remainder_y
      - .offset:         62
        .size:           2
        .value_kind:     hidden_remainder_z
      - .offset:         80
        .size:           8
        .value_kind:     hidden_global_offset_x
      - .offset:         88
        .size:           8
        .value_kind:     hidden_global_offset_y
      - .offset:         96
        .size:           8
        .value_kind:     hidden_global_offset_z
      - .offset:         104
        .size:           2
        .value_kind:     hidden_grid_dims
      - .offset:         160
        .size:           4
        .value_kind:     hidden_dynamic_lds_size
    .group_segment_fixed_size: 0
    .kernarg_segment_align: 8
    .kernarg_segment_size: 296
    .language:       OpenCL C
    .language_version:
      - 2
      - 0
    .max_flat_workgroup_size: 512
    .name:           _Z8k3t_mfmaILi1EEvPK15HIP_vector_typeIjLj4EEPKjS3_PKfPf
    .private_segment_fixed_size: 0
    .sgpr_count:     74
    .sgpr_spill_count: 0
    .symbol:         _Z8k3t_mfmaILi1EEvPK15HIP_vector_typeIjLj4EEPKjS3_PKfPf.kd
    .uniform_work_group_size: 1
    .uses_dynamic_stack: false
    .vgpr_count:     256
    .vgpr_spill_count: 0
    .wavefront_size: 64
